# MoE gather phase: row gather loop handles two rows per trip (8 loads in flight, counted waits) instead of load-wait-store per row
# speedup vs baseline: 1.0055x; 1.0055x over previous
; __global__ void __launch_bounds__(NWAVES * 64, 2) trunk_fwd(Args args) {
;     ...
;             for (int q = 2 * wave; q < npair; q += 2 * NWAVES) { const int m = r0 + (q >> 1);
;                 const v4u* src = (const v4u*)(Hb + (size_t)m * D); v4u* d0 = (v4u*)(HPERM + (size_t)SH[320 + q] * D); v4u* d1 = (v4u*)(HPERM + (size_t)SH[320 + q + 1] * D);
;                 v4u t[4];
; #pragma unroll
;                 for (int jj = 0; jj < 4; ++jj) t[jj] = src[lane + 64 * jj];
; #pragma unroll
;                 for (int jj = 0; jj < 4; ++jj) { d0[lane + 64 * jj] = t[jj]; d1[lane + 64 * jj] = t[jj]; } }
.LBB0_980:
	s_add_i32 s4, s0, 16
	s_cmp_ge_i32 s4, s7
	s_cbranch_scc1 .Lgather_one
	s_ashr_i32 s4, s0, 1
	s_add_i32 s4, s4, s6
	s_ashr_i32 s5, s4, 31
	s_lshl_b64 s[4:5], s[4:5], 12
	v_lshl_add_u64 v[18:19], v[2:3], 0, s[4:5]
	global_load_dwordx4 v[6:9], v[18:19], off
	global_load_dwordx4 v[10:13], v[18:19], off offset:1024
	global_load_dwordx4 v[14:17], v[18:19], off offset:2048
	global_load_dwordx4 v[200:203], v[18:19], off offset:3072
	s_mov_b64 s[4:5], 0x8000
	v_lshl_add_u64 v[18:19], v[18:19], 0, s[4:5]
	global_load_dwordx4 v[204:207], v[18:19], off
	global_load_dwordx4 v[208:211], v[18:19], off offset:1024
	global_load_dwordx4 v[212:215], v[18:19], off offset:2048
	global_load_dwordx4 v[216:219], v[18:19], off offset:3072
	v_mov_b32_e32 v1, s1
	ds_read_b64 v[22:23], v1
	ds_read_b64 v[220:221], v1 offset:64
	s_add_i32 s0, s0, 32
	s_addk_i32 s1, 0x80
	s_waitcnt lgkmcnt(0)
	v_ashrrev_i32_e32 v25, 31, v22
	v_mov_b32_e32 v24, v22
	v_ashrrev_i32_e32 v27, 31, v23
	v_mov_b32_e32 v26, v23
	v_lshlrev_b64 v[24:25], 12, v[24:25]
	v_lshlrev_b64 v[22:23], 12, v[26:27]
	v_lshl_add_u64 v[24:25], v[4:5], 0, v[24:25]
	v_lshl_add_u64 v[22:23], v[4:5], 0, v[22:23]
	v_ashrrev_i32_e32 v223, 31, v220
	v_mov_b32_e32 v222, v220
	v_ashrrev_i32_e32 v233, 31, v221
	v_mov_b32_e32 v232, v221
	v_lshlrev_b64 v[222:223], 12, v[222:223]
	v_lshlrev_b64 v[220:221], 12, v[232:233]
	v_lshl_add_u64 v[222:223], v[4:5], 0, v[222:223]
	v_lshl_add_u64 v[220:221], v[4:5], 0, v[220:221]
	s_waitcnt vmcnt(7)
	global_store_dwordx4 v[24:25], v[6:9], off
	global_store_dwordx4 v[22:23], v[6:9], off
	s_waitcnt vmcnt(8)
	global_store_dwordx4 v[24:25], v[10:13], off offset:1024
	global_store_dwordx4 v[22:23], v[10:13], off offset:1024
	s_waitcnt vmcnt(9)
	global_store_dwordx4 v[24:25], v[14:17], off offset:2048
	global_store_dwordx4 v[22:23], v[14:17], off offset:2048
	s_waitcnt vmcnt(10)
	global_store_dwordx4 v[24:25], v[200:203], off offset:3072
	global_store_dwordx4 v[22:23], v[200:203], off offset:3072
	s_waitcnt vmcnt(11)
	global_store_dwordx4 v[222:223], v[204:207], off
	global_store_dwordx4 v[220:221], v[204:207], off
	s_waitcnt vmcnt(12)
	global_store_dwordx4 v[222:223], v[208:211], off offset:1024
	global_store_dwordx4 v[220:221], v[208:211], off offset:1024
	s_waitcnt vmcnt(13)
	global_store_dwordx4 v[222:223], v[212:215], off offset:2048
	global_store_dwordx4 v[220:221], v[212:215], off offset:2048
	s_waitcnt vmcnt(14)
	global_store_dwordx4 v[222:223], v[216:219], off offset:3072
	global_store_dwordx4 v[220:221], v[216:219], off offset:3072
	s_cmp_ge_i32 s0, s7
	s_cbranch_scc0 .LBB0_980
	s_branch .LBB0_981
